# attention: barrier at each kind's tile-loop preheader closes a K-slot-0 reuse race between the first QK reads and the first loop trip's DMA (baseline latent race); plus earlier indexer/dilated-mask ch
# baseline (speedup 1.0000x reference)
.LBB0_1540:
	s_barrier
	s_nop 0
	s_lshl_b64 s[38:39], s[38:39], 1
	v_or_b32_e32 v139, s56, v4
	v_lshlrev_b32_e32 v4, 1, v137
	s_add_u32 s10, s10, s38
	v_and_b32_e32 v4, 32, v4
	s_addc_u32 s11, s11, s39
	v_lshlrev_b32_e32 v141, 2, v6
	v_add3_u32 v4, s68, v4, v5
	v_lshlrev_b32_e32 v5, 8, v6
	v_lshlrev_b32_e32 v6, 4, v137
	v_lshl_add_u64 v[134:135], s[10:11], 0, v[2:3]
	v_sub_u32_e32 v2, v136, v141
	v_and_b32_e32 v6, 0xc0, v6
	v_mov_b32_e32 v16, v3
	v_mov_b32_e32 v17, v3
	v_add3_u32 v142, v4, v5, v6
	v_lshl_add_u32 v143, v2, 2, s79
	v_add3_u32 v144, s68, v7, v8
	v_mov_b32_e32 v2, v3
	v_mov_b32_e32 v4, v3
	v_mov_b32_e32 v5, v3
	v_mov_b32_e32 v6, v3
	v_mov_b32_e32 v7, v3
	v_mov_b32_e32 v8, v3
	v_mov_b32_e32 v9, v3
	v_mov_b32_e32 v10, v3
	v_mov_b32_e32 v11, v3
	v_mov_b32_e32 v12, v3
	v_mov_b32_e32 v13, v3
	v_mov_b32_e32 v14, v3
	v_mov_b32_e32 v15, v3
	v_mov_b64_e32 v[34:35], v[16:17]
	v_mov_b64_e32 v[66:67], v[16:17]
	s_add_u32 s38, s4, s12
	v_mov_b64_e32 v[32:33], v[14:15]
	v_mov_b64_e32 v[30:31], v[12:13]
	v_mov_b64_e32 v[28:29], v[10:11]
	v_mov_b64_e32 v[26:27], v[8:9]
	v_mov_b64_e32 v[24:25], v[6:7]
	v_mov_b64_e32 v[22:23], v[4:5]
	v_mov_b64_e32 v[20:21], v[2:3]
	v_mov_b64_e32 v[64:65], v[14:15]
	v_mov_b64_e32 v[62:63], v[12:13]
	v_mov_b64_e32 v[60:61], v[10:11]
	v_mov_b64_e32 v[58:59], v[8:9]
	v_mov_b64_e32 v[56:57], v[6:7]
	v_mov_b64_e32 v[54:55], v[4:5]
	v_mov_b64_e32 v[52:53], v[2:3]
	v_mov_b64_e32 v[18:19], v[16:17]
	s_addc_u32 s39, s5, s13
	v_or_b32_e32 v140, s48, v137
	v_mov_b32_e32 v145, 0xf149f2ca
	s_mov_b32 s56, 0
	s_mov_b32 s57, 0
	v_mov_b64_e32 v[16:17], v[14:15]
	v_mov_b64_e32 v[14:15], v[12:13]
	v_mov_b64_e32 v[12:13], v[10:11]
	v_mov_b64_e32 v[10:11], v[8:9]
	v_mov_b64_e32 v[8:9], v[6:7]
	v_mov_b64_e32 v[6:7], v[4:5]
	v_mov_b64_e32 v[4:5], v[2:3]
	s_branch .LBB0_1543

.LBB0_1652:
	v_or_b32_e32 v4, s42, v170
	v_mov_b32_e32 v5, s81
	s_movk_i32 s4, 0x104
	v_mad_u32_u24 v174, v4, s4, v5
	v_lshlrev_b32_e32 v4, 10, v22
	v_lshlrev_b32_e32 v5, 4, v170
	v_add3_u32 v175, s68, v4, v5
	ds_read_b128 v[4:7], v175
	ds_read_b128 v[8:11], v175 offset:512
	ds_read_b128 v[12:15], v175 offset:2048
	ds_read_b128 v[16:19], v175 offset:2560
	ds_read_b128 v[24:27], v175 offset:4096
	ds_read_b128 v[28:31], v175 offset:4608
	ds_read_b128 v[32:35], v175 offset:6144
	ds_read_b128 v[36:39], v175 offset:6656
	s_bfe_u32 s91, s41, 0x10006
	s_waitcnt lgkmcnt(7)
	v_mfma_f32_32x32x16_bf16 v[52:67], v[4:7], v[148:151], 0
	s_mov_b32 s48, s49
	s_mov_b32 s50, s49
	s_mov_b32 s51, s49
	s_mov_b32 s52, s49
	s_mov_b32 s53, s49
	s_mov_b32 s54, s49
	s_mov_b32 s55, s49
	s_waitcnt lgkmcnt(6)
	v_mfma_f32_32x32x16_bf16 v[68:83], v[8:11], v[148:151], 0
	s_mov_b32 s56, s49
	s_mov_b32 s57, s49
	s_mov_b32 s58, s49
	s_mov_b32 s59, s49
	s_mov_b32 s60, s49
	s_mov_b32 s61, s49
	s_mov_b32 s62, s49
	s_waitcnt lgkmcnt(5)
	v_mfma_f32_32x32x16_bf16 v[52:67], v[12:15], v[152:155], v[52:67]
	s_mov_b32 s63, s49
	s_waitcnt lgkmcnt(4)
	v_mfma_f32_32x32x16_bf16 v[68:83], v[16:19], v[152:155], v[68:83]
	v_mov_b64_e32 v[4:5], s[48:49]
	v_mov_b64_e32 v[6:7], s[50:51]
	v_mov_b64_e32 v[8:9], s[52:53]
	v_mov_b64_e32 v[10:11], s[54:55]
	v_mov_b64_e32 v[12:13], s[56:57]
	v_mov_b64_e32 v[14:15], s[58:59]
	v_mov_b64_e32 v[16:17], s[60:61]
	s_waitcnt lgkmcnt(3)
	v_mfma_f32_32x32x16_bf16 v[52:67], v[24:27], v[156:159], v[52:67]
	v_mov_b64_e32 v[18:19], s[62:63]
	s_waitcnt lgkmcnt(2)
	v_mfma_f32_32x32x16_bf16 v[68:83], v[28:31], v[156:159], v[68:83]
	s_waitcnt lgkmcnt(1)
	v_mfma_f32_32x32x16_bf16 v[52:67], v[32:35], v[160:163], v[52:67]
	s_waitcnt lgkmcnt(0)
	v_mfma_f32_32x32x16_bf16 v[68:83], v[36:39], v[160:163], v[68:83]
	v_lshlrev_b32_e32 v21, 1, v21
	v_and_b32_e32 v21, 32, v21
	v_add3_u32 v20, s68, v21, v20
	v_lshlrev_b32_e32 v21, 8, v22
	v_and_b32_e32 v2, 0xc0, v2
	s_mulk_i32 s40, 0x2100
	v_lshlrev_b32_e32 v176, 2, v22
	v_add3_u32 v2, v20, v21, v2
	v_mov_b64_e32 v[34:35], v[18:19]
	v_mov_b64_e32 v[50:51], v[18:19]
	s_add_i32 s48, s70, s40
	s_mov_b32 s54, 1
	v_mov_b32_e32 v167, 0xf149f2ca
	s_mov_b32 s46, 0
	v_mov_b64_e32 v[32:33], v[16:17]
	v_mov_b64_e32 v[30:31], v[14:15]
	v_mov_b64_e32 v[28:29], v[12:13]
	v_mov_b64_e32 v[26:27], v[10:11]
	v_mov_b64_e32 v[24:25], v[8:9]
	v_mov_b64_e32 v[22:23], v[6:7]
	v_mov_b64_e32 v[20:21], v[4:5]
	s_mov_b32 s52, 0
	s_mov_b32 s53, 0
	v_mov_b64_e32 v[48:49], v[16:17]
	v_mov_b64_e32 v[46:47], v[14:15]
	v_mov_b64_e32 v[44:45], v[12:13]
	v_mov_b64_e32 v[42:43], v[10:11]
	v_mov_b64_e32 v[40:41], v[8:9]
	v_mov_b64_e32 v[38:39], v[6:7]
	v_mov_b64_e32 v[36:37], v[4:5]
	s_barrier
	s_nop 0
	s_branch .LBB0_1655

.LBB0_1791:
	s_barrier
	s_nop 0
	v_lshlrev_b32_e32 v2, 1, v19
	v_and_b32_e32 v2, 32, v2
	v_lshlrev_b32_e32 v5, 4, v19
	v_add3_u32 v2, s68, v2, v20
	v_lshlrev_b32_e32 v4, 8, v18
	v_and_b32_e32 v5, 0xc0, v5
	v_mov_b32_e32 v16, v3
	v_mov_b32_e32 v17, v3
	v_lshlrev_b32_e32 v159, 3, v18
	s_lshl_b32 s4, s82, 2
	v_lshlrev_b32_e32 v160, 2, v18
	v_add3_u32 v161, v2, v4, v5
	v_add3_u32 v162, s68, v21, v22
	v_mov_b32_e32 v2, v3
	v_mov_b32_e32 v4, v3
	v_mov_b32_e32 v5, v3
	v_mov_b32_e32 v6, v3
	v_mov_b32_e32 v7, v3
	v_mov_b32_e32 v8, v3
	v_mov_b32_e32 v9, v3
	v_mov_b32_e32 v10, v3
	v_mov_b32_e32 v11, v3
	v_mov_b32_e32 v12, v3
	v_mov_b32_e32 v13, v3
	v_mov_b32_e32 v14, v3
	v_mov_b32_e32 v15, v3
	v_mov_b64_e32 v[32:33], v[16:17]
	v_mov_b64_e32 v[48:49], v[16:17]
	v_mov_b64_e32 v[96:97], v[16:17]
	v_ashrrev_i32_e32 v155, 31, v154
	s_lshl_b32 s52, s6, 6
	s_mov_b32 s53, 2
	s_mov_b32 s36, 3
	s_or_b32 s54, s4, 3
	s_mov_b32 s59, 1
	v_mov_b32_e32 v163, 0xf149f2ca
	s_mov_b32 s58, 0
	v_mov_b64_e32 v[30:31], v[14:15]
	v_mov_b64_e32 v[28:29], v[12:13]
	v_mov_b64_e32 v[26:27], v[10:11]
	v_mov_b64_e32 v[24:25], v[8:9]
	v_mov_b64_e32 v[22:23], v[6:7]
	v_mov_b64_e32 v[20:21], v[4:5]
	v_mov_b64_e32 v[18:19], v[2:3]
	v_mov_b64_e32 v[46:47], v[14:15]
	v_mov_b64_e32 v[44:45], v[12:13]
	v_mov_b64_e32 v[42:43], v[10:11]
	v_mov_b64_e32 v[40:41], v[8:9]
	v_mov_b64_e32 v[38:39], v[6:7]
	v_mov_b64_e32 v[36:37], v[4:5]
	v_mov_b64_e32 v[34:35], v[2:3]
	s_mov_b32 s55, 0
	s_mov_b32 s56, 0
	v_mov_b64_e32 v[94:95], v[14:15]
	v_mov_b64_e32 v[92:93], v[12:13]
	v_mov_b64_e32 v[90:91], v[10:11]
	v_mov_b64_e32 v[88:89], v[8:9]
	v_mov_b64_e32 v[86:87], v[6:7]
	v_mov_b64_e32 v[84:85], v[4:5]
	v_mov_b64_e32 v[82:83], v[2:3]
	s_branch .LBB0_1794

.LBB0_1836:
	s_barrier
	s_nop 0
	v_lshlrev_b32_e32 v2, 1, v19
	s_add_u32 s7, s51, s50
	v_and_b32_e32 v2, 32, v2
	v_lshlrev_b32_e32 v5, 4, v19
	s_addc_u32 s37, s55, s5
	v_add3_u32 v2, s68, v2, v20
	v_lshlrev_b32_e32 v4, 8, v18
	v_and_b32_e32 v5, 0xc0, v5
	v_mov_b32_e32 v16, v3
	v_mov_b32_e32 v17, v3
	s_add_u32 s55, s42, s46
	v_lshlrev_b32_e32 v188, 2, v18
	v_add3_u32 v189, v2, v4, v5
	v_mov_b32_e32 v2, v3
	v_mov_b32_e32 v4, v3
	v_mov_b32_e32 v5, v3
	v_mov_b32_e32 v6, v3
	v_mov_b32_e32 v7, v3
	v_mov_b32_e32 v8, v3
	v_mov_b32_e32 v9, v3
	v_mov_b32_e32 v10, v3
	v_mov_b32_e32 v11, v3
	v_mov_b32_e32 v12, v3
	v_mov_b32_e32 v13, v3
	v_mov_b32_e32 v14, v3
	v_mov_b32_e32 v15, v3
	v_mov_b64_e32 v[32:33], v[16:17]
	v_mov_b64_e32 v[48:49], v[16:17]
	v_mov_b64_e32 v[64:65], v[16:17]
	s_addc_u32 s56, s43, s47
	v_mov_b32_e32 v181, 0xf149f2ca
	s_mov_b32 s57, 0
	v_mov_b64_e32 v[30:31], v[14:15]
	v_mov_b64_e32 v[28:29], v[12:13]
	v_mov_b64_e32 v[26:27], v[10:11]
	v_mov_b64_e32 v[24:25], v[8:9]
	v_mov_b64_e32 v[22:23], v[6:7]
	v_mov_b64_e32 v[20:21], v[4:5]
	v_mov_b64_e32 v[18:19], v[2:3]
	v_mov_b64_e32 v[46:47], v[14:15]
	v_mov_b64_e32 v[44:45], v[12:13]
	v_mov_b64_e32 v[42:43], v[10:11]
	v_mov_b64_e32 v[40:41], v[8:9]
	v_mov_b64_e32 v[38:39], v[6:7]
	v_mov_b64_e32 v[36:37], v[4:5]
	v_mov_b64_e32 v[34:35], v[2:3]
	s_mov_b32 s58, 0
	v_mov_b64_e32 v[62:63], v[14:15]
	v_mov_b64_e32 v[60:61], v[12:13]
	v_mov_b64_e32 v[58:59], v[10:11]
	v_mov_b64_e32 v[56:57], v[8:9]
	v_mov_b64_e32 v[54:55], v[6:7]
	v_mov_b64_e32 v[52:53], v[4:5]
	v_mov_b64_e32 v[50:51], v[2:3]
	s_branch .LBB0_1839
